# baseline (speedup 1.0000x reference)
.Lk1p_o:
	s_mov_b64 exec, s[8:9]
	ds_read_b32 v16, v16
	ds_read_b32 v17, v17
	ds_read_b32 v18, v18
	ds_read_b32 v19, v19
	ds_read_b32 v20, v20
	ds_read_b32 v21, v21
	ds_read_b32 v22, v22
	ds_read_b32 v23, v23
	s_waitcnt lgkmcnt(0)
	v_add_u32_e32 v4, v16, v48
	v_lshlrev_b32_e32 v4, 2, v4
	ds_write_b32 v4, v32 offset:4352
	v_add_u32_e32 v5, v17, v49
	v_lshlrev_b32_e32 v5, 2, v5
	ds_write_b32 v5, v33 offset:4352
	v_add_u32_e32 v6, v18, v50
	v_lshlrev_b32_e32 v6, 2, v6
	ds_write_b32 v6, v34 offset:4352
	v_add_u32_e32 v7, v19, v51
	v_lshlrev_b32_e32 v7, 2, v7
	ds_write_b32 v7, v35 offset:4352
	v_add_u32_e32 v4, v20, v52
	v_lshlrev_b32_e32 v4, 2, v4
	ds_write_b32 v4, v36 offset:4352
	v_add_u32_e32 v5, v21, v53
	v_lshlrev_b32_e32 v5, 2, v5
	ds_write_b32 v5, v37 offset:4352
	v_add_u32_e32 v6, v22, v54
	v_lshlrev_b32_e32 v6, 2, v6
	ds_write_b32 v6, v38 offset:4352
	v_add_u32_e32 v7, v23, v55
	v_lshlrev_b32_e32 v7, 2, v7
	ds_write_b32 v7, v39 offset:4352
	s_waitcnt lgkmcnt(0)
	s_barrier
	s_sub_u32 s16, 0xf4240, s3
	s_min_u32 s16, s16, 0x2000
	v_lshlrev_b32_e32 v4, 2, v0
	v_lshlrev_b32_e32 v5, 4, v0
	ds_read_b128 v[16:19], v5 offset:4352
	ds_read_b128 v[20:23], v5 offset:20736
	s_lshl_b32 s17, s3, 2
	v_add_u32_e32 v6, s17, v5
	v_add_u32_e32 v7, 0x1000, v4
	v_add_u32_e32 v8, 0x4000, v6
	v_cmp_gt_u32_e32 vcc, s16, v4
	v_cmp_gt_u32_e64 s[8:9], s16, v7
	s_waitcnt lgkmcnt(0)
	s_mov_b64 exec, vcc
	s_cbranch_execz .LBB0_98
	global_store_dwordx4 v6, v[16:19], s[12:13] sc1
	s_mov_b64 exec, s[8:9]
	s_cbranch_execz .LBB0_98
	global_store_dwordx4 v8, v[20:23], s[12:13] sc1
